# code placement: the five GEMM K-loop heads aligned to 64 bytes (s_nop padding executed once per loop entry)
# baseline (speedup 1.0000x reference)
; __device__ __forceinline__ int tid_opaque() { int t = threadIdx.x; asm volatile("" : "+v"(t)); return t; }
; #define G8_STAGE(P, BASE, LD, br, kt) G8_STAGE_X(tid, P, BASE, LD, br, kt)
; #define G8_WAIT_V(n) asm volatile("s_waitcnt vmcnt(" #n ")" ::: "memory")
; #define G8_BAR __builtin_amdgcn_s_barrier()
; __device__ __forceinline__ void gemm8_kloop(f32x4 (&acc)[2][2][4][2], char* shm_, const bf16_t* A, long lda, const bf16_t* Bt, long ldb, int nt) {
;     ...
;     const int tid = tid_opaque(); int wid = tid >> 6, lane = tid & 63, wr = wid >> 2, wc = wid & 3, fr = lane & 15, fq = lane >> 4;
;     bf16x8 At[4][2], B0[2][2], B1[2][2];
;     if (wr == 1) G8_BAR;
;     G8_WAIT_V(4); G8_BAR;
;     G8_STAGE(G8_SB(1, 0), Bt, ldb, 0, 1); G8_STAGE(G8_SA(1, 0), A, lda, 0, 1); G8_STAGE(G8_SB(1, 1), Bt, ldb, 128, 1);
.LBB0_187:
	s_or_b64 exec, exec, s[28:29]
	v_ashrrev_i32_e32 v4, 31, v3
	v_lshrrev_b32_e32 v4, 26, v4
	v_add_u32_e32 v4, v3, v4
	v_ashrrev_i32_e32 v5, 6, v4
	v_bfe_i32 v4, v3, 27, 1
	v_lshlrev_b32_e32 v130, 4, v3
	v_lshrrev_b32_e32 v4, 22, v4
	v_add_u32_e32 v4, v130, v4
	v_and_b32_e32 v4, 0xfffffc00, v4
	v_sub_u32_e32 v4, v130, v4
	v_lshrrev_b32_e32 v6, 4, v4
	s_ashr_i32 s74, s2, 5
	s_lshl_b32 s29, s2, 5
	v_bitop3_b32 v6, v6, v4, 32 bitop3:0x6c
	v_ashrrev_i32_e32 v4, 31, v4
	s_and_b32 s0, s70, 7
	s_and_b32 s28, s74, -8
	s_and_b32 s71, s29, 0x1f00
	s_and_b32 s29, s2, 7
	v_lshrrev_b32_e32 v4, 26, v4
	s_lshl_b32 s73, s0, 8
	s_lshl_b32 s0, s3, 12
	s_or_b32 s72, s28, s29
	v_lshlrev_b32_e32 v7, 3, v5
	v_add_u32_e32 v4, v6, v4
	s_and_b32 s0, s0, 0x1f00000
	s_lshl_b32 s60, s72, 8
	s_lshl_b32 s28, s71, 12
	v_and_b32_e32 v7, -16, v7
	v_ashrrev_i32_e32 v8, 6, v4
	s_add_u32 s58, s36, s28
	v_add_u32_e32 v4, v8, v7
	v_mul_i32_i24_e32 v7, 64, v8
	s_addc_u32 s59, s37, 0
	s_ashr_i32 s61, s60, 31
	s_mul_i32 s28, s72, 0x108000
	v_lshlrev_b32_e32 v5, 5, v5
	v_sub_u32_e32 v6, v6, v7
	s_mul_hi_i32 s29, s60, 0x1080
	s_add_u32 s62, s56, s28
	v_and_b32_e32 v5, 32, v5
	v_ashrrev_i16_sdwa v6, v140, sext(v6) dst_sel:DWORD dst_unused:UNUSED_PAD src0_sel:DWORD src1_sel:BYTE_0
	s_addc_u32 s63, s57, s29
	v_add_u32_sdwa v6, v5, sext(v6) dst_sel:DWORD dst_unused:UNUSED_PAD src0_sel:DWORD src1_sel:WORD_0
	v_mov_b64_e32 v[8:9], s[62:63]
	v_ashrrev_i32_e32 v7, 31, v6
	v_mad_i64_i32 v[10:11], s[28:29], v4, s19, v[8:9]
	v_lshlrev_b64 v[6:7], 1, v[6:7]
	v_add_u32_e32 v141, s55, v130
	v_lshl_add_u64 v[10:11], v[10:11], 0, v[6:7]
	v_readfirstlane_b32 s28, v141
	v_lshl_add_u64 v[10:11], v[10:11], 0, s[4:5]
	s_mov_b32 m0, s28
	v_add_u32_e32 v22, 0x2000, v130
	s_waitcnt vmcnt(4)
	s_barrier
; __device__ __forceinline__ int tid_opaque() { int t = threadIdx.x; asm volatile("" : "+v"(t)); return t; }
; #define G8_STAGE(P, BASE, LD, br, kt) G8_STAGE_X(tid, P, BASE, LD, br, kt)
; #define G8_WAIT_V(n) asm volatile("s_waitcnt vmcnt(" #n ")" ::: "memory")
; #define G8_BAR __builtin_amdgcn_s_barrier()
; __device__ __forceinline__ void gemm8_kloop(f32x4 (&acc)[2][2][4][2], char* shm_, const bf16_t* A, long lda, const bf16_t* Bt, long ldb, int nt) {
;     ...
;     const int tid = tid_opaque(); int wid = tid >> 6, lane = tid & 63, wr = wid >> 2, wc = wid & 3, fr = lane & 15, fq = lane >> 4;
;     bf16x8 At[4][2], B0[2][2], B1[2][2];
;     if (wr == 1) G8_BAR;
;     G8_WAIT_V(4); G8_BAR;
;     G8_STAGE(G8_SB(1, 0), Bt, ldb, 0, 1); G8_STAGE(G8_SA(1, 0), A, lda, 0, 1); G8_STAGE(G8_SB(1, 1), Bt, ldb, 128, 1);
;     G8_WAIT_V(6); G8_BAR;
	global_load_lds_dwordx4 v[10:11], off
	v_ashrrev_i32_e32 v10, 31, v22
	v_lshrrev_b32_e32 v10, 22, v10
	v_add_u32_e32 v10, v22, v10
	v_ashrrev_i32_e32 v11, 10, v10
	v_mul_i32_i24_e32 v10, 0x400, v11
	v_sub_u32_e32 v10, v22, v10
	v_lshrrev_b32_e32 v12, 4, v10
	v_bitop3_b32 v12, v12, v10, 32 bitop3:0x6c
	v_ashrrev_i32_e32 v13, 31, v12
	v_lshrrev_b32_e32 v13, 26, v13
	v_add_u32_e32 v13, v12, v13
	v_ashrrev_i32_e32 v14, 6, v13
	v_and_b32_e32 v13, 0xc0, v13
	v_lshlrev_b32_e32 v10, 3, v11
	v_lshlrev_b32_e32 v11, 5, v11
	v_sub_u32_e32 v12, v12, v13
	v_and_b32_e32 v11, 32, v11
	v_ashrrev_i16_sdwa v12, v140, sext(v12) dst_sel:DWORD dst_unused:UNUSED_PAD src0_sel:DWORD src1_sel:BYTE_0
	v_and_b32_e32 v10, -16, v10
	v_add_u32_sdwa v12, v11, sext(v12) dst_sel:DWORD dst_unused:UNUSED_PAD src0_sel:DWORD src1_sel:WORD_0
	v_add_u32_e32 v10, v14, v10
	v_ashrrev_i32_e32 v13, 31, v12
	v_mad_i64_i32 v[8:9], s[28:29], v10, s19, v[8:9]
	v_lshlrev_b64 v[12:13], 1, v[12:13]
	v_add_u32_e32 v14, s55, v22
	v_lshl_add_u64 v[8:9], v[8:9], 0, v[12:13]
	v_readfirstlane_b32 s28, v14
	v_ashrrev_i32_e32 v5, 31, v4
	v_lshl_add_u64 v[8:9], v[8:9], 0, s[4:5]
	s_mov_b32 m0, s28
	v_add_u32_e32 v142, 0, v130
	global_load_lds_dwordx4 v[8:9], off
	v_lshlrev_b64 v[8:9], 12, v[4:5]
	v_lshl_add_u64 v[14:15], s[58:59], 0, v[8:9]
	v_add_u32_e32 v143, 0x8000, v142
	v_lshl_add_u64 v[14:15], v[14:15], 0, v[6:7]
	v_readfirstlane_b32 s28, v143
	v_ashrrev_i32_e32 v11, 31, v10
	v_lshl_add_u64 v[14:15], v[14:15], 0, s[4:5]
	s_mov_b32 m0, s28
	v_add_u32_e32 v144, 0xa000, v142
	global_load_lds_dwordx4 v[14:15], off
	v_lshlrev_b64 v[14:15], 12, v[10:11]
	v_lshl_add_u64 v[16:17], s[58:59], 0, v[14:15]
	v_readfirstlane_b32 s28, v144
	v_lshl_add_u64 v[16:17], v[16:17], 0, v[12:13]
	s_mov_b32 m0, s28
	s_add_u32 s28, s62, 0x84080
	v_lshl_add_u64 v[16:17], v[16:17], 0, s[4:5]
	s_addc_u32 s29, s63, 0
	global_load_lds_dwordx4 v[16:17], off
	v_mov_b64_e32 v[16:17], s[28:29]
	v_mad_i64_i32 v[18:19], s[28:29], v4, s19, v[16:17]
	v_add_u32_e32 v145, s64, v130
	v_add_u32_e32 v5, s64, v22
	v_readfirstlane_b32 s28, v145
	s_mov_b32 m0, s28
	v_mad_i64_i32 v[16:17], s[28:29], v10, s19, v[16:17]
	v_lshl_add_u64 v[18:19], v[18:19], 0, v[6:7]
	v_readfirstlane_b32 s28, v5
	global_load_lds_dwordx4 v[18:19], off
	v_lshl_add_u64 v[16:17], v[16:17], 0, v[12:13]
	s_mov_b32 m0, s28
	v_and_b32_e32 v20, 15, v3
	global_load_lds_dwordx4 v[16:17], off
	v_and_b32_e32 v21, 48, v3
	v_lshlrev_b32_e32 v11, 2, v3
	v_lshlrev_b32_e32 v3, 6, v3
	s_movk_i32 s28, 0x3c0
	v_lshlrev_b32_e32 v22, 13, v2
	v_and_or_b32 v2, v3, s28, v21
	s_lshl_b32 s28, s74, 8
	v_lshlrev_b32_e32 v5, 6, v20
	v_and_b32_e32 v11, 32, v11
	s_and_b32 s28, s28, 0xfffff800
	v_bitop3_b32 v5, v5, v11, v21 bitop3:0x36
	v_and_b32_e32 v20, 0x3000, v3
	v_xad_u32 v11, v2, v11, 0
	s_or_b32 s62, s28, s73
	v_mad_i64_i32 v[2:3], s[28:29], v4, s19, 0
	v_mad_i64_i32 v[2:3], s[28:29], s62, v1, v[2:3]
	v_lshl_add_u64 v[132:133], v[2:3], 0, v[6:7]
	v_mad_i64_i32 v[2:3], s[28:29], v10, s19, 0
	v_mad_i64_i32 v[2:3], s[28:29], s62, v1, v[2:3]
	v_lshl_add_u64 v[134:135], v[2:3], 0, v[12:13]
	v_lshl_add_u64 v[2:3], s[0:1], 0, v[8:9]
	s_waitcnt vmcnt(6)
	v_lshl_add_u64 v[136:137], v[2:3], 0, v[6:7]
	v_lshl_add_u64 v[2:3], s[0:1], 0, v[14:15]
	v_add_u32_e32 v16, s65, v5
	v_add_u32_e32 v17, s68, v5
	v_add_u32_e32 v18, s55, v5
	v_add_u32_e32 v19, s64, v5
	v_add_u32_e32 v5, 0, v5
	v_or_b32_e32 v21, 0x800, v22
	v_or_b32_e32 v23, 0x1000, v22
	v_or_b32_e32 v24, 0x1800, v22
	v_lshl_add_u64 v[138:139], v[2:3], 0, v[12:13]
	v_mov_b32_e32 v2, 0
	s_mov_b32 s0, -2
	v_add_u32_e32 v146, v16, v20
	v_add_u32_e32 v147, v5, v22
	v_add_u32_e32 v148, v11, v21
	v_add_u32_e32 v149, v11, v23
	v_add_u32_e32 v150, v11, v24
	v_add_u32_e32 v151, v17, v20
	v_add_u32_e32 v152, v18, v20
	v_add_u32_e32 v153, v19, v20
	v_mov_b32_e32 v3, v2
	v_mov_b32_e32 v4, v2
	v_mov_b32_e32 v5, v2
	v_mov_b32_e32 v6, v2
	v_mov_b32_e32 v7, v2
	v_mov_b32_e32 v8, v2
	v_mov_b32_e32 v9, v2
	v_mov_b32_e32 v10, v2
	v_mov_b32_e32 v11, v2
	v_mov_b32_e32 v12, v2
	v_mov_b32_e32 v13, v2
	v_mov_b32_e32 v14, v2
	v_mov_b32_e32 v15, v2
	v_mov_b32_e32 v16, v2
	v_mov_b32_e32 v17, v2
	v_mov_b32_e32 v18, v2
	v_mov_b32_e32 v19, v2
	v_mov_b32_e32 v20, v2
	v_mov_b32_e32 v21, v2
	v_mov_b32_e32 v22, v2
	v_mov_b32_e32 v23, v2
	v_mov_b32_e32 v24, v2
	v_mov_b32_e32 v25, v2
	v_mov_b32_e32 v26, v2
	v_mov_b32_e32 v27, v2
	v_mov_b32_e32 v28, v2
	v_mov_b32_e32 v29, v2
	v_mov_b32_e32 v30, v2
	v_mov_b32_e32 v31, v2
	v_mov_b32_e32 v32, v2
	v_mov_b32_e32 v33, v2
	v_mov_b32_e32 v34, v2
	v_mov_b32_e32 v35, v2
	v_mov_b32_e32 v36, v2
	v_mov_b32_e32 v37, v2
	v_mov_b32_e32 v38, v2
	v_mov_b32_e32 v39, v2
	v_mov_b32_e32 v40, v2
	v_mov_b32_e32 v41, v2
	v_mov_b32_e32 v42, v2
	v_mov_b32_e32 v43, v2
	v_mov_b32_e32 v44, v2
	v_mov_b32_e32 v45, v2
	v_mov_b32_e32 v46, v2
	v_mov_b32_e32 v47, v2
	v_mov_b32_e32 v48, v2
	v_mov_b32_e32 v49, v2
	v_mov_b32_e32 v50, v2
	v_mov_b32_e32 v51, v2
	v_mov_b32_e32 v52, v2
	v_mov_b32_e32 v53, v2
	v_mov_b32_e32 v54, v2
	v_mov_b32_e32 v55, v2
	v_mov_b32_e32 v56, v2
	v_mov_b32_e32 v57, v2
	v_mov_b32_e32 v58, v2
	v_mov_b32_e32 v59, v2
	v_mov_b32_e32 v60, v2
	v_mov_b32_e32 v61, v2
	v_mov_b32_e32 v62, v2
	v_mov_b32_e32 v63, v2
	v_mov_b32_e32 v64, v2
	v_mov_b32_e32 v65, v2
	v_mov_b32_e32 v66, v2
	v_mov_b32_e32 v67, v2
	v_mov_b32_e32 v68, v2
	v_mov_b32_e32 v69, v2
	v_mov_b32_e32 v70, v2
	v_mov_b32_e32 v71, v2
	v_mov_b32_e32 v72, v2
	v_mov_b32_e32 v73, v2
	v_mov_b32_e32 v74, v2
	v_mov_b32_e32 v75, v2
	v_mov_b32_e32 v76, v2
	v_mov_b32_e32 v77, v2
	v_mov_b32_e32 v78, v2
	v_mov_b32_e32 v79, v2
	v_mov_b32_e32 v80, v2
	v_mov_b32_e32 v81, v2
	v_mov_b32_e32 v82, v2
	v_mov_b32_e32 v83, v2
	v_mov_b32_e32 v84, v2
	v_mov_b32_e32 v85, v2
	v_mov_b32_e32 v86, v2
	v_mov_b32_e32 v87, v2
	v_mov_b32_e32 v88, v2
	v_mov_b32_e32 v89, v2
	v_mov_b32_e32 v90, v2
	v_mov_b32_e32 v91, v2
	v_mov_b32_e32 v92, v2
	v_mov_b32_e32 v93, v2
	v_mov_b32_e32 v94, v2
	v_mov_b32_e32 v95, v2
	v_mov_b32_e32 v96, v2
	v_mov_b32_e32 v97, v2
	v_mov_b32_e32 v98, v2
	v_mov_b32_e32 v99, v2
	v_mov_b32_e32 v100, v2
	v_mov_b32_e32 v101, v2
	v_mov_b32_e32 v102, v2
	v_mov_b32_e32 v103, v2
	v_mov_b32_e32 v104, v2
	v_mov_b32_e32 v105, v2
	v_mov_b32_e32 v106, v2
	v_mov_b32_e32 v107, v2
	v_mov_b32_e32 v108, v2
	v_mov_b32_e32 v109, v2
	v_mov_b32_e32 v110, v2
	v_mov_b32_e32 v111, v2
	v_mov_b32_e32 v112, v2
	v_mov_b32_e32 v113, v2
	v_mov_b32_e32 v114, v2
	v_mov_b32_e32 v115, v2
	v_mov_b32_e32 v116, v2
	v_mov_b32_e32 v117, v2
	v_mov_b32_e32 v118, v2
	v_mov_b32_e32 v119, v2
	v_mov_b32_e32 v120, v2
	v_mov_b32_e32 v121, v2
	v_mov_b32_e32 v122, v2
	v_mov_b32_e32 v123, v2
	v_mov_b32_e32 v124, v2
	v_mov_b32_e32 v125, v2
	v_mov_b32_e32 v126, v2
	v_mov_b32_e32 v127, v2
	v_mov_b32_e32 v128, v2
	v_mov_b32_e32 v129, v2
	v_add_u32_e32 v154, 0xc000, v142
	v_add_u32_e32 v155, 0xe000, v142
	s_barrier
	.p2alignl 6, 3212836864

; __device__ __forceinline__ int tid_opaque() { int t = threadIdx.x; asm volatile("" : "+v"(t)); return t; }
; #define G8_STAGE(P, BASE, LD, br, kt) G8_STAGE_X(tid, P, BASE, LD, br, kt)
; #define G8_WAIT_V(n) asm volatile("s_waitcnt vmcnt(" #n ")" ::: "memory")
; #define G8_BAR __builtin_amdgcn_s_barrier()
; __device__ __forceinline__ void gemm8_kloop(f32x4 (&acc)[2][2][4][2], char* shm_, const bf16_t* A, long lda, const bf16_t* Bt, long ldb, int nt) {
;     ...
;     const int tid = tid_opaque(); int wid = tid >> 6, lane = tid & 63, wr = wid >> 2, wc = wid & 3, fr = lane & 15, fq = lane >> 4;
;     bf16x8 At[4][2], B0[2][2], B1[2][2];
;     if (wr == 1) G8_BAR;
;     G8_WAIT_V(4); G8_BAR;
;     G8_STAGE(G8_SB(1, 0), Bt, ldb, 0, 1); G8_STAGE(G8_SA(1, 0), A, lda, 0, 1); G8_STAGE(G8_SB(1, 1), Bt, ldb, 128, 1);
;     G8_WAIT_V(6); G8_BAR;
; __device__ __forceinline__ void phase_merge(const Ptrs& p, LAS unsigned char* lds) {
;     ...
;         for (int seg = 0; seg < 2; ++seg) {
;             gemm8_kloop(acc, (char*)lds, ua + (size_t)row0 * 2048 + seg * 1024, 2048, (seg ? wtao : wtco) + (size_t)col0 * WTP1, WTP1, 1024 / 64);
.LBB0_513:
	s_or_b64 exec, exec, s[0:1]
	v_ashrrev_i32_e32 v22, 31, v21
	v_lshrrev_b32_e32 v22, 26, v22
	v_add_u32_e32 v22, v21, v22
	v_ashrrev_i32_e32 v23, 6, v22
	v_bfe_i32 v22, v21, 27, 1
	v_lshlrev_b32_e32 v2, 4, v21
	v_lshrrev_b32_e32 v22, 22, v22
	v_add_u32_e32 v22, v2, v22
	v_and_b32_e32 v22, 0xfffffc00, v22
	v_sub_u32_e32 v22, v2, v22
	v_lshrrev_b32_e32 v136, 4, v22
	v_bitop3_b32 v136, v136, v22, 32 bitop3:0x6c
	v_ashrrev_i32_e32 v22, 31, v22
	s_xor_b64 s[0:1], s[6:7], -1
	s_lshl_b64 vcc, s[4:5], 1
	v_lshrrev_b32_e32 v22, 26, v22
	s_add_u32 s4, s84, vcc_lo
	v_lshlrev_b32_e32 v137, 3, v23
	v_add_u32_e32 v22, v136, v22
	s_addc_u32 s5, s85, vcc_hi
	v_and_b32_e32 v137, -16, v137
	v_ashrrev_i32_e32 v138, 6, v22
	s_and_b64 s[78:79], s[6:7], exec
	v_add_u32_e32 v22, v138, v137
	v_mul_i32_i24_e32 v137, 64, v138
	s_cselect_b32 s92, s22, s24
	v_lshlrev_b32_e32 v23, 5, v23
	v_sub_u32_e32 v136, v136, v137
	s_cselect_b32 s19, s23, s25
	s_add_u32 s78, s92, s18
	v_and_b32_e32 v23, 32, v23
	v_ashrrev_i16_sdwa v136, v1, sext(v136) dst_sel:DWORD dst_unused:UNUSED_PAD src0_sel:DWORD src1_sel:BYTE_0
	s_addc_u32 s79, s19, 0
	v_add_u32_sdwa v136, v23, sext(v136) dst_sel:DWORD dst_unused:UNUSED_PAD src0_sel:DWORD src1_sel:WORD_0
	v_mov_b64_e32 v[138:139], s[78:79]
	v_ashrrev_i32_e32 v137, 31, v136
	s_waitcnt vmcnt(0)
	v_mad_i64_i32 v[140:141], s[90:91], v22, s69, v[138:139]
	v_lshlrev_b64 v[136:137], 1, v[136:137]
	v_lshl_add_u64 v[140:141], v[140:141], 0, v[136:137]
	v_add_u32_e32 v156, 0x2000, v2
	v_lshl_add_u64 v[142:143], v[140:141], 0, s[16:17]
	v_ashrrev_i32_e32 v141, 31, v156
	v_add_u32_e32 v140, s72, v2
	v_lshrrev_b32_e32 v141, 22, v141
	v_readfirstlane_b32 s90, v140
	v_add_u32_e32 v141, v156, v141
	s_mov_b32 m0, s90
	v_ashrrev_i32_e32 v141, 10, v141
	s_waitcnt vmcnt(4)
	s_barrier
	global_load_lds_dwordx4 v[142:143], off
	v_mul_i32_i24_e32 v142, 0x400, v141
	v_sub_u32_e32 v142, v156, v142
	v_lshrrev_b32_e32 v143, 4, v142
	v_bitop3_b32 v142, v143, v142, 32 bitop3:0x6c
	v_ashrrev_i32_e32 v144, 31, v142
	v_lshrrev_b32_e32 v144, 26, v144
	v_lshlrev_b32_e32 v143, 3, v141
	v_add_u32_e32 v144, v142, v144
	v_and_b32_e32 v143, -16, v143
	v_ashrrev_i32_e32 v145, 6, v144
	v_add_u32_e32 v146, v145, v143
	v_and_b32_e32 v143, 0xc0, v144
	v_lshlrev_b32_e32 v141, 5, v141
	v_sub_u32_e32 v142, v142, v143
	v_and_b32_e32 v141, 32, v141
	v_ashrrev_i16_sdwa v142, v1, sext(v142) dst_sel:DWORD dst_unused:UNUSED_PAD src0_sel:DWORD src1_sel:BYTE_0
	v_add_u32_sdwa v142, v141, sext(v142) dst_sel:DWORD dst_unused:UNUSED_PAD src0_sel:DWORD src1_sel:WORD_0
	v_ashrrev_i32_e32 v143, 31, v142
	v_mad_i64_i32 v[138:139], s[90:91], v146, s69, v[138:139]
	v_lshlrev_b64 v[148:149], 1, v[142:143]
	v_add_u32_e32 v141, s72, v156
	v_lshl_add_u64 v[138:139], v[138:139], 0, v[148:149]
	v_readfirstlane_b32 s90, v141
	v_ashrrev_i32_e32 v23, 31, v22
	v_lshl_add_u64 v[138:139], v[138:139], 0, s[16:17]
	s_mov_b32 m0, s90
	v_add_u32_e32 v141, 0, v2
	global_load_lds_dwordx4 v[138:139], off
	v_lshlrev_b64 v[138:139], 12, v[22:23]
	v_lshl_add_u64 v[142:143], s[4:5], 0, v[138:139]
	v_lshl_add_u64 v[142:143], v[142:143], 0, v[136:137]
	v_lshl_add_u64 v[144:145], v[142:143], 0, s[16:17]
	v_add_u32_e32 v142, 0x8000, v141
	v_ashrrev_i32_e32 v147, 31, v146
	v_readfirstlane_b32 s90, v142
	s_mov_b32 m0, s90
	v_lshlrev_b64 v[150:151], 12, v[146:147]
	global_load_lds_dwordx4 v[144:145], off
	v_lshl_add_u64 v[144:145], s[4:5], 0, v[150:151]
	v_add_u32_e32 v143, 0xa000, v141
	s_add_u32 s78, s78, 0x44080
	v_lshl_add_u64 v[144:145], v[144:145], 0, v[148:149]
	v_readfirstlane_b32 s90, v143
	s_addc_u32 s79, s79, 0
	v_lshl_add_u64 v[144:145], v[144:145], 0, s[16:17]
	s_mov_b32 m0, s90
	v_mov_b64_e32 v[152:153], s[78:79]
	global_load_lds_dwordx4 v[144:145], off
	v_mad_i64_i32 v[144:145], s[78:79], v22, s69, v[152:153]
	v_lshl_add_u64 v[154:155], v[144:145], 0, v[136:137]
	v_add_u32_e32 v144, s73, v2
	v_add_u32_e32 v23, s73, v156
	v_readfirstlane_b32 s78, v144
	s_mov_b32 m0, s78
	v_mad_i64_i32 v[152:153], s[78:79], v146, s69, v[152:153]
	v_readfirstlane_b32 s78, v23
	global_load_lds_dwordx4 v[154:155], off
	v_lshl_add_u64 v[152:153], v[152:153], 0, v[148:149]
	s_mov_b32 m0, s78
	v_and_b32_e32 v23, 15, v21
	global_load_lds_dwordx4 v[152:153], off
	v_and_b32_e32 v145, 48, v21
	v_lshlrev_b32_e32 v147, 2, v21
	v_lshlrev_b32_e32 v21, 6, v21
	s_movk_i32 s78, 0x3c0
	v_lshlrev_b32_e32 v23, 6, v23
	v_and_b32_e32 v147, 32, v147
	v_lshlrev_b32_e32 v157, 13, v20
	v_and_or_b32 v20, v21, s78, v145
	v_lshl_add_u64 v[138:139], v[138:139], 0, vcc
	s_waitcnt vmcnt(6)
	v_bitop3_b32 v23, v23, v147, v145 bitop3:0x36
	v_and_b32_e32 v156, 0x3000, v21
	v_xad_u32 v159, v20, v147, 0
	s_add_u32 s78, s92, s83
	v_mad_i64_i32 v[20:21], s[90:91], v22, s69, v[136:137]
	v_lshl_add_u64 v[136:137], v[138:139], 0, v[136:137]
	v_lshl_add_u64 v[138:139], v[150:151], 0, vcc
	v_add_u32_e32 v152, s70, v23
	v_add_u32_e32 v153, s71, v23
	v_add_u32_e32 v154, s72, v23
	v_add_u32_e32 v155, s73, v23
	v_add_u32_e32 v158, 0, v23
	v_or_b32_e32 v147, 0x800, v157
	v_or_b32_e32 v160, 0x1000, v157
	v_or_b32_e32 v161, 0x1800, v157
	s_addc_u32 s79, s19, 0
	v_mad_i64_i32 v[22:23], s[90:91], v146, s69, v[148:149]
	v_lshl_add_u64 v[138:139], v[138:139], 0, v[148:149]
	v_lshl_add_u64 v[20:21], s[78:79], 0, v[20:21]
	v_lshl_add_u64 v[22:23], s[78:79], 0, v[22:23]
	v_lshl_add_u64 v[136:137], s[34:35], 0, v[136:137]
	v_lshl_add_u64 v[138:139], s[34:35], 0, v[138:139]
	s_mov_b32 s19, -2
	s_mov_b64 vcc, 0
	v_add_u32_e32 v145, v152, v156
	v_add_u32_e32 v146, v158, v157
	v_add_u32_e32 v147, v159, v147
	v_add_u32_e32 v148, v159, v160
	v_add_u32_e32 v149, v159, v161
	v_add_u32_e32 v150, v153, v156
	v_add_u32_e32 v151, v154, v156
	v_add_u32_e32 v152, v155, v156
	s_barrier
	.p2alignl 6, 3212836864

; __device__ __forceinline__ int tid_opaque() { int t = threadIdx.x; asm volatile("" : "+v"(t)); return t; }
; __device__ __forceinline__ int vwg_id() { const int G = gridDim.x; return (G % 8 == 0) ? (int)((blockIdx.x % 8) * (G / 8) + blockIdx.x / 8) : (int)blockIdx.x; }
; #define G8_WAIT_V(n) asm volatile("s_waitcnt vmcnt(" #n ")" ::: "memory")
; #define G8_BAR __builtin_amdgcn_s_barrier()
; __device__ __forceinline__ void gemm8_kloop(f32x4 (&acc)[2][2][4][2], char* shm_, const bf16_t* A, long lda, const bf16_t* Bt, long ldb, int nt) {
;     ...
;     const int tid = tid_opaque(); int wid = tid >> 6, lane = tid & 63, wr = wid >> 2, wc = wid & 3, fr = lane & 15, fq = lane >> 4;
;     bf16x8 At[4][2], B0[2][2], B1[2][2];
;     if (wr == 1) G8_BAR;
;     G8_WAIT_V(4); G8_BAR;
; __device__ __forceinline__ void phase_out(const Ptrs& p, LAS unsigned char* lds) {
;     ...
;         if (u == vwg_id()) gemm8_issue0((char*)lds, mg + (size_t)row0 * D, D, wto + (size_t)col0 * WTP2, WTP2);
;         gemm8_kloop(acc, (char*)lds, mg + (size_t)row0 * D, D, wto + (size_t)col0 * WTP2, WTP2, D / 64);
.LBB0_845:
	s_or_b64 exec, exec, s[28:29]
	v_ashrrev_i32_e32 v4, 31, v3
	v_lshrrev_b32_e32 v4, 26, v4
	v_add_u32_e32 v4, v3, v4
	v_ashrrev_i32_e32 v5, 6, v4
	v_bfe_i32 v4, v3, 27, 1
	v_lshlrev_b32_e32 v138, 4, v3
	v_lshrrev_b32_e32 v4, 22, v4
	v_add_u32_e32 v4, v138, v4
	v_and_b32_e32 v4, 0xfffffc00, v4
	v_sub_u32_e32 v4, v138, v4
	v_lshrrev_b32_e32 v6, 4, v4
	v_bitop3_b32 v6, v6, v4, 32 bitop3:0x6c
	v_ashrrev_i32_e32 v4, 31, v4
	v_lshrrev_b32_e32 v4, 26, v4
	v_lshlrev_b32_e32 v7, 3, v5
	v_add_u32_e32 v4, v6, v4
	v_and_b32_e32 v7, -16, v7
	v_ashrrev_i32_e32 v8, 6, v4
	s_add_u32 s38, s12, s38
	v_add_u32_e32 v4, v8, v7
	v_mul_i32_i24_e32 v7, 64, v8
	s_addc_u32 s39, s13, s39
	s_lshl_b64 s[54:55], s[0:1], 1
	v_lshlrev_b32_e32 v5, 5, v5
	v_sub_u32_e32 v6, v6, v7
	s_add_u32 s58, s76, s54
	v_and_b32_e32 v5, 32, v5
	v_ashrrev_i16_sdwa v6, v1, sext(v6) dst_sel:DWORD dst_unused:UNUSED_PAD src0_sel:DWORD src1_sel:BYTE_0
	s_addc_u32 s59, s77, s55
	s_and_b32 s28, s18, 0xffffff00
	v_add_u32_sdwa v6, v5, sext(v6) dst_sel:DWORD dst_unused:UNUSED_PAD src0_sel:DWORD src1_sel:WORD_0
	s_ashr_i32 s29, s28, 31
	v_mov_b64_e32 v[8:9], s[58:59]
	v_ashrrev_i32_e32 v7, 31, v6
	s_lshl_b64 s[56:57], s[28:29], 12
	v_mad_i64_i32 v[10:11], s[28:29], v4, s60, v[8:9]
	v_lshlrev_b64 v[6:7], 1, v[6:7]
	v_add_u32_e32 v139, s63, v138
	v_lshl_add_u64 v[10:11], v[10:11], 0, v[6:7]
	v_readfirstlane_b32 s0, v139
	v_lshl_add_u64 v[10:11], v[10:11], 0, s[4:5]
	s_mov_b32 m0, s0
	v_add_u32_e32 v22, 0x2000, v138
	s_waitcnt vmcnt(4)
	s_barrier
; __device__ __forceinline__ int tid_opaque() { int t = threadIdx.x; asm volatile("" : "+v"(t)); return t; }
; #define G8_STAGE(P, BASE, LD, br, kt) G8_STAGE_X(tid, P, BASE, LD, br, kt)
; #define G8_WAIT_V(n) asm volatile("s_waitcnt vmcnt(" #n ")" ::: "memory")
; #define G8_BAR __builtin_amdgcn_s_barrier()
; #define G8_ZERO(acc) do { _Pragma("unroll") for (int a_ = 0; a_ < 2; ++a_) _Pragma("unroll") for (int b_ = 0; b_ < 2; ++b_) _Pragma("unroll") for (int m_ = 0; m_ < 4; ++m_) _Pragma("unroll") for (int n_ = 0; n_ < 2; ++n_) acc[a_][b_][m_][n_] = (f32x4){0.f, 0.f, 0.f, 0.f}; } while (0)
; __device__ __forceinline__ void gemm8_kloop(f32x4 (&acc)[2][2][4][2], char* shm_, const bf16_t* A, long lda, const bf16_t* Bt, long ldb, int nt) {
;     ...
;     const int tid = tid_opaque(); int wid = tid >> 6, lane = tid & 63, wr = wid >> 2, wc = wid & 3, fr = lane & 15, fq = lane >> 4;
;     bf16x8 At[4][2], B0[2][2], B1[2][2];
;     if (wr == 1) G8_BAR;
;     G8_WAIT_V(4); G8_BAR;
;     G8_STAGE(G8_SB(1, 0), Bt, ldb, 0, 1); G8_STAGE(G8_SA(1, 0), A, lda, 0, 1); G8_STAGE(G8_SB(1, 1), Bt, ldb, 128, 1);
;     G8_WAIT_V(6); G8_BAR;
; __device__ __forceinline__ void phase_out(const Ptrs& p, LAS unsigned char* lds) {
;     ...
;         f32x4 acc[2][2][4][2]; G8_ZERO(acc);
	global_load_lds_dwordx4 v[10:11], off
	v_ashrrev_i32_e32 v10, 31, v22
	v_lshrrev_b32_e32 v10, 22, v10
	v_add_u32_e32 v10, v22, v10
	v_ashrrev_i32_e32 v11, 10, v10
	v_mul_i32_i24_e32 v10, 0x400, v11
	v_sub_u32_e32 v10, v22, v10
	v_lshrrev_b32_e32 v12, 4, v10
	v_bitop3_b32 v12, v12, v10, 32 bitop3:0x6c
	v_ashrrev_i32_e32 v13, 31, v12
	v_lshrrev_b32_e32 v13, 26, v13
	v_add_u32_e32 v13, v12, v13
	v_ashrrev_i32_e32 v14, 6, v13
	v_and_b32_e32 v13, 0xc0, v13
	v_lshlrev_b32_e32 v10, 3, v11
	v_lshlrev_b32_e32 v11, 5, v11
	v_sub_u32_e32 v12, v12, v13
	v_and_b32_e32 v11, 32, v11
	v_ashrrev_i16_sdwa v12, v1, sext(v12) dst_sel:DWORD dst_unused:UNUSED_PAD src0_sel:DWORD src1_sel:BYTE_0
	v_and_b32_e32 v10, -16, v10
	v_add_u32_sdwa v12, v11, sext(v12) dst_sel:DWORD dst_unused:UNUSED_PAD src0_sel:DWORD src1_sel:WORD_0
	v_add_u32_e32 v10, v14, v10
	v_ashrrev_i32_e32 v13, 31, v12
	v_mad_i64_i32 v[8:9], s[28:29], v10, s60, v[8:9]
	v_lshlrev_b64 v[12:13], 1, v[12:13]
	v_add_u32_e32 v14, s63, v22
	v_lshl_add_u64 v[8:9], v[8:9], 0, v[12:13]
	v_readfirstlane_b32 s0, v14
	v_ashrrev_i32_e32 v5, 31, v4
	v_lshl_add_u64 v[8:9], v[8:9], 0, s[4:5]
	s_mov_b32 m0, s0
	s_waitcnt vmcnt(0)
	v_add_u32_e32 v140, 0, v138
	global_load_lds_dwordx4 v[8:9], off
	v_lshlrev_b64 v[8:9], 12, v[4:5]
	v_lshl_add_u64 v[14:15], s[38:39], 0, v[8:9]
	v_add_u32_e32 v141, 0x8000, v140
	v_lshl_add_u64 v[14:15], v[14:15], 0, v[6:7]
	v_readfirstlane_b32 s0, v141
	v_ashrrev_i32_e32 v11, 31, v10
	v_lshl_add_u64 v[14:15], v[14:15], 0, s[4:5]
	s_mov_b32 m0, s0
	v_add_u32_e32 v142, 0xa000, v140
	global_load_lds_dwordx4 v[14:15], off
	v_lshlrev_b64 v[14:15], 12, v[10:11]
	v_lshl_add_u64 v[16:17], s[38:39], 0, v[14:15]
	v_lshl_add_u64 v[16:17], v[16:17], 0, v[12:13]
	v_readfirstlane_b32 s0, v142
	s_add_u32 s28, s58, 0x84080
	v_lshl_add_u64 v[16:17], v[16:17], 0, s[4:5]
	s_mov_b32 m0, s0
	s_addc_u32 s29, s59, 0
	global_load_lds_dwordx4 v[16:17], off
	v_mov_b64_e32 v[16:17], s[28:29]
	v_add_u32_e32 v143, s64, v138
	v_mad_i64_i32 v[18:19], s[28:29], v4, s60, v[16:17]
	v_readfirstlane_b32 s0, v143
	v_add_u32_e32 v5, s64, v22
	v_lshl_add_u64 v[18:19], v[18:19], 0, v[6:7]
	s_mov_b32 m0, s0
	v_mad_i64_i32 v[16:17], s[28:29], v10, s60, v[16:17]
	v_readfirstlane_b32 s0, v5
	global_load_lds_dwordx4 v[18:19], off
	v_lshl_add_u64 v[16:17], v[16:17], 0, v[12:13]
	s_mov_b32 m0, s0
	v_and_b32_e32 v20, 15, v3
	global_load_lds_dwordx4 v[16:17], off
	v_and_b32_e32 v21, 48, v3
	v_lshlrev_b32_e32 v11, 2, v3
	v_lshlrev_b32_e32 v3, 6, v3
	v_lshlrev_b32_e32 v5, 6, v20
	v_and_b32_e32 v11, 32, v11
	v_lshlrev_b32_e32 v22, 13, v2
	v_and_or_b32 v2, v3, s65, v21
	v_bitop3_b32 v5, v5, v11, v21 bitop3:0x36
	v_and_b32_e32 v20, 0x3000, v3
	v_xad_u32 v11, v2, v11, 0
	v_mov_b64_e32 v[2:3], s[54:55]
	v_add_u32_e32 v16, s61, v5
	v_add_u32_e32 v17, s62, v5
	v_add_u32_e32 v18, s63, v5
	v_add_u32_e32 v19, s64, v5
	v_add_u32_e32 v23, 0, v5
	v_mad_i64_i32 v[4:5], s[28:29], v4, s60, v[2:3]
	v_mad_i64_i32 v[2:3], s[28:29], v10, s60, v[2:3]
	v_lshl_add_u64 v[132:133], v[2:3], 0, v[12:13]
	v_lshl_add_u64 v[2:3], s[56:57], 0, v[8:9]
	s_waitcnt vmcnt(6)
	v_lshl_add_u64 v[134:135], v[2:3], 0, v[6:7]
	v_lshl_add_u64 v[2:3], s[56:57], 0, v[14:15]
	v_or_b32_e32 v21, 0x800, v22
	v_or_b32_e32 v24, 0x1000, v22
	v_or_b32_e32 v25, 0x1800, v22
	v_lshl_add_u64 v[136:137], v[2:3], 0, v[12:13]
	v_mov_b32_e32 v2, 0
	v_lshl_add_u64 v[130:131], v[4:5], 0, v[6:7]
	s_mov_b32 s0, -2
	v_add_u32_e32 v144, v16, v20
	v_add_u32_e32 v145, v23, v22
	v_add_u32_e32 v146, v11, v21
	v_add_u32_e32 v147, v11, v24
	v_add_u32_e32 v148, v11, v25
	v_add_u32_e32 v149, v17, v20
	v_add_u32_e32 v150, v18, v20
	v_add_u32_e32 v151, v19, v20
	v_mov_b32_e32 v3, v2
	v_mov_b32_e32 v4, v2
	v_mov_b32_e32 v5, v2
	v_mov_b32_e32 v6, v2
	v_mov_b32_e32 v7, v2
	v_mov_b32_e32 v8, v2
	v_mov_b32_e32 v9, v2
	v_mov_b32_e32 v10, v2
	v_mov_b32_e32 v11, v2
	v_mov_b32_e32 v12, v2
	v_mov_b32_e32 v13, v2
	v_mov_b32_e32 v14, v2
	v_mov_b32_e32 v15, v2
	v_mov_b32_e32 v16, v2
	v_mov_b32_e32 v17, v2
	v_mov_b32_e32 v18, v2
	v_mov_b32_e32 v19, v2
	v_mov_b32_e32 v20, v2
	v_mov_b32_e32 v21, v2
	v_mov_b32_e32 v22, v2
	v_mov_b32_e32 v23, v2
	v_mov_b32_e32 v24, v2
	v_mov_b32_e32 v25, v2
	v_mov_b32_e32 v26, v2
	v_mov_b32_e32 v27, v2
	v_mov_b32_e32 v28, v2
	v_mov_b32_e32 v29, v2
	v_mov_b32_e32 v30, v2
	v_mov_b32_e32 v31, v2
	v_mov_b32_e32 v32, v2
	v_mov_b32_e32 v33, v2
	v_mov_b32_e32 v34, v2
	v_mov_b32_e32 v35, v2
	v_mov_b32_e32 v36, v2
	v_mov_b32_e32 v37, v2
	v_mov_b32_e32 v38, v2
	v_mov_b32_e32 v39, v2
	v_mov_b32_e32 v40, v2
	v_mov_b32_e32 v41, v2
	v_mov_b32_e32 v42, v2
	v_mov_b32_e32 v43, v2
	v_mov_b32_e32 v44, v2
	v_mov_b32_e32 v45, v2
	v_mov_b32_e32 v46, v2
	v_mov_b32_e32 v47, v2
	v_mov_b32_e32 v48, v2
	v_mov_b32_e32 v49, v2
	v_mov_b32_e32 v50, v2
	v_mov_b32_e32 v51, v2
	v_mov_b32_e32 v52, v2
	v_mov_b32_e32 v53, v2
	v_mov_b32_e32 v54, v2
	v_mov_b32_e32 v55, v2
	v_mov_b32_e32 v56, v2
	v_mov_b32_e32 v57, v2
	v_mov_b32_e32 v58, v2
	v_mov_b32_e32 v59, v2
	v_mov_b32_e32 v60, v2
	v_mov_b32_e32 v61, v2
	v_mov_b32_e32 v62, v2
	v_mov_b32_e32 v63, v2
	v_mov_b32_e32 v64, v2
	v_mov_b32_e32 v65, v2
	v_mov_b32_e32 v66, v2
	v_mov_b32_e32 v67, v2
	v_mov_b32_e32 v68, v2
	v_mov_b32_e32 v69, v2
	v_mov_b32_e32 v70, v2
	v_mov_b32_e32 v71, v2
	v_mov_b32_e32 v72, v2
	v_mov_b32_e32 v73, v2
	v_mov_b32_e32 v74, v2
	v_mov_b32_e32 v75, v2
	v_mov_b32_e32 v76, v2
	v_mov_b32_e32 v77, v2
	v_mov_b32_e32 v78, v2
	v_mov_b32_e32 v79, v2
	v_mov_b32_e32 v80, v2
	v_mov_b32_e32 v81, v2
	v_mov_b32_e32 v82, v2
	v_mov_b32_e32 v83, v2
	v_mov_b32_e32 v84, v2
	v_mov_b32_e32 v85, v2
	v_mov_b32_e32 v86, v2
	v_mov_b32_e32 v87, v2
	v_mov_b32_e32 v88, v2
	v_mov_b32_e32 v89, v2
	v_mov_b32_e32 v90, v2
	v_mov_b32_e32 v91, v2
	v_mov_b32_e32 v92, v2
	v_mov_b32_e32 v93, v2
	v_mov_b32_e32 v94, v2
	v_mov_b32_e32 v95, v2
	v_mov_b32_e32 v96, v2
	v_mov_b32_e32 v97, v2
	v_mov_b32_e32 v98, v2
	v_mov_b32_e32 v99, v2
	v_mov_b32_e32 v100, v2
	v_mov_b32_e32 v101, v2
	v_mov_b32_e32 v102, v2
	v_mov_b32_e32 v103, v2
	v_mov_b32_e32 v104, v2
	v_mov_b32_e32 v105, v2
	v_mov_b32_e32 v106, v2
	v_mov_b32_e32 v107, v2
	v_mov_b32_e32 v108, v2
	v_mov_b32_e32 v109, v2
	v_mov_b32_e32 v110, v2
	v_mov_b32_e32 v111, v2
	v_mov_b32_e32 v112, v2
	v_mov_b32_e32 v113, v2
	v_mov_b32_e32 v114, v2
	v_mov_b32_e32 v115, v2
	v_mov_b32_e32 v116, v2
	v_mov_b32_e32 v117, v2
	v_mov_b32_e32 v118, v2
	v_mov_b32_e32 v119, v2
	v_mov_b32_e32 v120, v2
	v_mov_b32_e32 v121, v2
	v_mov_b32_e32 v122, v2
	v_mov_b32_e32 v123, v2
	v_mov_b32_e32 v124, v2
	v_mov_b32_e32 v125, v2
	v_mov_b32_e32 v126, v2
	v_mov_b32_e32 v127, v2
	v_mov_b32_e32 v128, v2
	v_mov_b32_e32 v129, v2
	s_barrier
	.p2alignl 6, 3212836864

; #define G_DMA_A(buf, t, i_) __builtin_amdgcn_raw_ptr_buffer_load_lds(ra, (LAS void*)(lds + (buf) * 65536 + a_wu + (i_) * 8192), 16, ao##i_, (unsigned)(t) * 128u, 0, 0)
; #define G_ISSUE_B(t) do { const unsigned so_ = (unsigned)(t) * 64u * ldbB; _Pragma("unroll") for (int i_ = 0; i_ < 8; ++i_) sb[i_] = __builtin_bit_cast(f32x4, __builtin_amdgcn_raw_buffer_load_b128(rb, bo, so_ + (unsigned)i_ * ldbB, 0)); } while (0)
; #define G_RETIRE() asm volatile("s_waitcnt vmcnt(0)" : "+v"(sb[0]), "+v"(sb[1]), "+v"(sb[2]), "+v"(sb[3]), "+v"(sb[4]), "+v"(sb[5]), "+v"(sb[6]), "+v"(sb[7]) :: "memory")
; #define G_WRITE_B(buf) do { LAS unsigned char* d_ = lds + (buf) * 65536; \
;         _Pragma("unroll") for (int j_ = 0; j_ < 4; ++j_) { u32x4 w_; w_.x = cvtpk(sb[0][j_], sb[1][j_]); w_.y = cvtpk(sb[2][j_], sb[3][j_]); w_.z = cvtpk(sb[4][j_], sb[5][j_]); w_.w = cvtpk(sb[6][j_], sb[7][j_]); \
;             *(LAS u32x4*)(d_ + 32768 + T.b_w + ((T.b_rot + 64u * j_) & 255u)) = w_; } } while (0)
; #define G_BAR() do { asm volatile("s_waitcnt lgkmcnt(0)" ::: "memory"); __builtin_amdgcn_s_barrier(); asm volatile("" ::: "memory"); } while (0)
; #define G_DMA_A(buf, t, i_) __builtin_amdgcn_raw_ptr_buffer_load_lds(ra, (LAS void*)(lds + (buf) * 65536 + a_wu + (i_) * 8192), 16, ao##i_, (unsigned)(t) * 128u, 0, 0)
; #define G_ISSUE_B(t) do { const unsigned so_ = (unsigned)(t) * 64u * ldbB; _Pragma("unroll") for (int i_ = 0; i_ < 8; ++i_) sb[i_] = __builtin_bit_cast(f32x4, __builtin_amdgcn_raw_buffer_load_b128(rb, bo, so_ + (unsigned)i_ * ldbB, 0)); } while (0)
; #define G_RETIRE() asm volatile("s_waitcnt vmcnt(0)" : "+v"(sb[0]), "+v"(sb[1]), "+v"(sb[2]), "+v"(sb[3]), "+v"(sb[4]), "+v"(sb[5]), "+v"(sb[6]), "+v"(sb[7]) :: "memory")
; __device__ __forceinline__ void gemm_kloop(f32x4 (&acc)[8][4], LAS unsigned char* lds, const GemmT& T, ...
;     ...
;     G_ISSUE_B(0); G_DMA_A(0, 0, 0); G_DMA_A(0, 0, 1); G_DMA_A(0, 0, 2); G_DMA_A(0, 0, 3); G_RETIRE(); G_WRITE_B(0);
;     if (nt > 1) G_ISSUE_B(1);
;     G_BAR();
; __device__ __forceinline__ void phase_moe_gu(const Ptrs& p, LAS unsigned char* lds) {
;     ...
;         f32x4 acc[8][4]; acc_zero(acc);
.LBB0_1263:
	s_cbranch_execz .LBB0_1267
	v_readfirstlane_b32 s1, v229
	s_and_b32 s1, s1, 0xfffffc00
	s_add_i32 s1, s1, 0
	s_mov_b32 s38, s26
	s_mov_b32 s39, s27
	s_mov_b32 m0, s1
	v_add_u32_e32 v3, v227, v218
	buffer_load_dwordx4 v223, s[36:39], 0 offen lds
	s_add_i32 m0, s1, 0x2000
	v_mov_b32_e32 v36, 0
	buffer_load_dwordx4 v222, s[36:39], 0 offen lds
	s_add_i32 m0, s1, 0x4000
	s_mov_b32 s3, 0
	buffer_load_dwordx4 v221, s[36:39], 0 offen lds
	s_add_i32 m0, s1, 0x6000
	s_mov_b32 s4, 0x10e000
	buffer_load_dwordx4 v224, s[36:39], 0 offen lds
	s_waitcnt vmcnt(4)
	s_waitcnt vmcnt(0)
	s_movk_i32 s5, 0x80
	v_cvt_pk_bf16_f32 v4, v114, v126
	v_cvt_pk_bf16_f32 v5, v130, v118
	v_cvt_pk_bf16_f32 v6, v122, v134
	v_cvt_pk_bf16_f32 v7, v142, v146
	ds_write_b128 v228, v[4:7] offset:32768
	v_cvt_pk_bf16_f32 v4, v115, v127
	v_cvt_pk_bf16_f32 v5, v131, v119
	v_cvt_pk_bf16_f32 v6, v123, v135
	v_cvt_pk_bf16_f32 v7, v143, v147
	ds_write_b128 v228, v[4:7] offset:32832
	v_cvt_pk_bf16_f32 v4, v116, v128
	v_cvt_pk_bf16_f32 v5, v132, v120
	v_cvt_pk_bf16_f32 v6, v124, v136
	v_cvt_pk_bf16_f32 v7, v144, v148
	ds_write_b128 v228, v[4:7] offset:32896
	v_cvt_pk_bf16_f32 v4, v117, v129
	v_cvt_pk_bf16_f32 v5, v133, v121
	v_cvt_pk_bf16_f32 v6, v125, v137
	v_cvt_pk_bf16_f32 v7, v145, v149
	ds_write_b128 v3, v[4:7] offset:32768
	buffer_load_dwordx4 v[4:7], v225, s[24:27], s67 offen
	buffer_load_dwordx4 v[8:11], v225, s[24:27], s76 offen
	buffer_load_dwordx4 v[12:15], v225, s[24:27], s77 offen
	buffer_load_dwordx4 v[16:19], v225, s[24:27], s78 offen
	buffer_load_dwordx4 v[20:23], v225, s[24:27], s79 offen
	buffer_load_dwordx4 v[28:31], v225, s[24:27], s80 offen
	buffer_load_dwordx4 v[24:27], v225, s[24:27], s81 offen
	buffer_load_dwordx4 v[32:35], v225, s[24:27], s82 offen
	s_waitcnt lgkmcnt(0)
	s_barrier
	v_mov_b32_e32 v37, v36
	v_mov_b32_e32 v38, v36
	v_mov_b32_e32 v39, v36
	v_mov_b32_e32 v40, v36
	v_mov_b32_e32 v41, v36
	v_mov_b32_e32 v42, v36
	v_mov_b32_e32 v43, v36
	v_mov_b32_e32 v44, v36
	v_mov_b32_e32 v45, v36
	v_mov_b32_e32 v46, v36
	v_mov_b32_e32 v47, v36
	v_mov_b32_e32 v48, v36
	v_mov_b32_e32 v49, v36
	v_mov_b32_e32 v50, v36
	v_mov_b32_e32 v51, v36
	v_mov_b32_e32 v52, v36
	v_mov_b32_e32 v53, v36
	v_mov_b32_e32 v54, v36
	v_mov_b32_e32 v55, v36
	v_mov_b32_e32 v56, v36
	v_mov_b32_e32 v57, v36
	v_mov_b32_e32 v58, v36
	v_mov_b32_e32 v59, v36
	v_mov_b32_e32 v60, v36
	v_mov_b32_e32 v61, v36
	v_mov_b32_e32 v62, v36
	v_mov_b32_e32 v63, v36
	v_mov_b32_e32 v64, v36
	v_mov_b32_e32 v65, v36
	v_mov_b32_e32 v66, v36
	v_mov_b32_e32 v67, v36
	v_mov_b32_e32 v68, v36
	v_mov_b32_e32 v69, v36
	v_mov_b32_e32 v70, v36
	v_mov_b32_e32 v71, v36
	v_mov_b32_e32 v72, v36
	v_mov_b32_e32 v73, v36
	v_mov_b32_e32 v74, v36
	v_mov_b32_e32 v75, v36
	v_mov_b32_e32 v76, v36
	v_mov_b32_e32 v77, v36
	v_mov_b32_e32 v78, v36
	v_mov_b32_e32 v79, v36
	v_mov_b32_e32 v80, v36
	v_mov_b32_e32 v81, v36
	v_mov_b32_e32 v82, v36
	v_mov_b32_e32 v83, v36
	v_mov_b32_e32 v84, v36
	v_mov_b32_e32 v85, v36
	v_mov_b32_e32 v86, v36
	v_mov_b32_e32 v87, v36
	v_mov_b32_e32 v88, v36
	v_mov_b32_e32 v89, v36
	v_mov_b32_e32 v90, v36
	v_mov_b32_e32 v91, v36
	v_mov_b32_e32 v92, v36
	v_mov_b32_e32 v93, v36
	v_mov_b32_e32 v94, v36
	v_mov_b32_e32 v95, v36
	v_mov_b32_e32 v96, v36
	v_mov_b32_e32 v97, v36
	v_mov_b32_e32 v98, v36
	v_mov_b32_e32 v99, v36
	v_mov_b32_e32 v100, v36
	v_mov_b32_e32 v101, v36
	v_mov_b32_e32 v102, v36
	v_mov_b32_e32 v103, v36
	v_mov_b32_e32 v104, v36
	v_mov_b32_e32 v105, v36
	v_mov_b32_e32 v106, v36
	v_mov_b32_e32 v107, v36
	v_mov_b32_e32 v108, v36
	v_mov_b32_e32 v109, v36
	v_mov_b32_e32 v110, v36
	v_mov_b32_e32 v111, v36
	v_mov_b32_e32 v112, v36
	v_mov_b32_e32 v113, v36
	v_mov_b32_e32 v114, v36
	v_mov_b32_e32 v115, v36
	v_mov_b32_e32 v116, v36
	v_mov_b32_e32 v117, v36
	v_mov_b32_e32 v118, v36
	v_mov_b32_e32 v119, v36
	v_mov_b32_e32 v120, v36
	v_mov_b32_e32 v121, v36
	v_mov_b32_e32 v122, v36
	v_mov_b32_e32 v123, v36
	v_mov_b32_e32 v124, v36
	v_mov_b32_e32 v125, v36
	v_mov_b32_e32 v126, v36
	v_mov_b32_e32 v127, v36
	v_mov_b32_e32 v128, v36
	v_mov_b32_e32 v129, v36
	v_mov_b32_e32 v130, v36
	v_mov_b32_e32 v131, v36
	v_mov_b32_e32 v132, v36
	v_mov_b32_e32 v133, v36
	v_mov_b32_e32 v134, v36
	v_mov_b32_e32 v135, v36
	v_mov_b32_e32 v136, v36
	v_mov_b32_e32 v137, v36
	v_mov_b32_e32 v138, v36
	v_mov_b32_e32 v139, v36
	v_mov_b32_e32 v140, v36
	v_mov_b32_e32 v141, v36
	v_mov_b32_e32 v142, v36
	v_mov_b32_e32 v143, v36
	v_mov_b32_e32 v144, v36
	v_mov_b32_e32 v145, v36
	v_mov_b32_e32 v146, v36
	v_mov_b32_e32 v147, v36
	v_mov_b32_e32 v148, v36
	v_mov_b32_e32 v149, v36
	v_mov_b32_e32 v150, v36
	v_mov_b32_e32 v151, v36
	v_mov_b32_e32 v152, v36
	v_mov_b32_e32 v153, v36
	v_mov_b32_e32 v154, v36
	v_mov_b32_e32 v155, v36
	v_mov_b32_e32 v156, v36
	v_mov_b32_e32 v157, v36
	v_mov_b32_e32 v158, v36
	v_mov_b32_e32 v159, v36
	v_mov_b32_e32 v160, v36
	v_mov_b32_e32 v161, v36
	v_mov_b32_e32 v162, v36
	v_mov_b32_e32 v163, v36
	.p2alignl 6, 3212836864

; #define G_DMA_A(buf, t, i_) __builtin_amdgcn_raw_ptr_buffer_load_lds(ra, (LAS void*)(lds + (buf) * 65536 + a_wu + (i_) * 8192), 16, ao##i_, (unsigned)(t) * 128u, 0, 0)
; #define G_ISSUE_B(t) do { const unsigned so_ = (unsigned)(t) * 64u * ldbB; _Pragma("unroll") for (int i_ = 0; i_ < 8; ++i_) sb[i_] = __builtin_bit_cast(f32x4, __builtin_amdgcn_raw_buffer_load_b128(rb, bo, so_ + (unsigned)i_ * ldbB, 0)); } while (0)
; #define G_RETIRE() asm volatile("s_waitcnt vmcnt(0)" : "+v"(sb[0]), "+v"(sb[1]), "+v"(sb[2]), "+v"(sb[3]), "+v"(sb[4]), "+v"(sb[5]), "+v"(sb[6]), "+v"(sb[7]) :: "memory")
; #define G_WRITE_B(buf) do { LAS unsigned char* d_ = lds + (buf) * 65536; \
;         _Pragma("unroll") for (int j_ = 0; j_ < 4; ++j_) { u32x4 w_; w_.x = cvtpk(sb[0][j_], sb[1][j_]); w_.y = cvtpk(sb[2][j_], sb[3][j_]); w_.z = cvtpk(sb[4][j_], sb[5][j_]); w_.w = cvtpk(sb[6][j_], sb[7][j_]); \
;             *(LAS u32x4*)(d_ + 32768 + T.b_w + ((T.b_rot + 64u * j_) & 255u)) = w_; } } while (0)
; #define G_BAR() do { asm volatile("s_waitcnt lgkmcnt(0)" ::: "memory"); __builtin_amdgcn_s_barrier(); asm volatile("" ::: "memory"); } while (0)
; #define G_DMA_A(buf, t, i_) __builtin_amdgcn_raw_ptr_buffer_load_lds(ra, (LAS void*)(lds + (buf) * 65536 + a_wu + (i_) * 8192), 16, ao##i_, (unsigned)(t) * 128u, 0, 0)
; #define G_ISSUE_B(t) do { const unsigned so_ = (unsigned)(t) * 64u * ldbB; _Pragma("unroll") for (int i_ = 0; i_ < 8; ++i_) sb[i_] = __builtin_bit_cast(f32x4, __builtin_amdgcn_raw_buffer_load_b128(rb, bo, so_ + (unsigned)i_ * ldbB, 0)); } while (0)
; #define G_RETIRE() asm volatile("s_waitcnt vmcnt(0)" : "+v"(sb[0]), "+v"(sb[1]), "+v"(sb[2]), "+v"(sb[3]), "+v"(sb[4]), "+v"(sb[5]), "+v"(sb[6]), "+v"(sb[7]) :: "memory")
; __device__ __forceinline__ void gemm_kloop(f32x4 (&acc)[8][4], LAS unsigned char* lds, const GemmT& T, ...
;     ...
;     G_ISSUE_B(0); G_DMA_A(0, 0, 0); G_DMA_A(0, 0, 1); G_DMA_A(0, 0, 2); G_DMA_A(0, 0, 3); G_RETIRE(); G_WRITE_B(0);
;     if (nt > 1) G_ISSUE_B(1);
;     G_BAR();
; __device__ __forceinline__ void phase_moe_down(const Ptrs& p, LAS unsigned char* lds) {
;     ...
;         f32x4 acc[8][4]; acc_zero(acc);
.LBB0_1574:
	s_cbranch_execz .LBB0_1578
	v_readfirstlane_b32 s1, v230
	s_and_b32 s1, s1, 0xfffffc00
	s_add_i32 s1, s1, 0
	s_mov_b32 s38, s26
	s_mov_b32 s39, s27
	s_mov_b32 m0, s1
	v_add_u32_e32 v3, v228, v221
	buffer_load_dwordx4 v225, s[36:39], 0 offen lds
	s_add_i32 m0, s1, 0x2000
	v_mov_b32_e32 v36, 0
	buffer_load_dwordx4 v226, s[36:39], 0 offen lds
	s_add_i32 m0, s1, 0x4000
	s_mov_b32 s2, 0
	buffer_load_dwordx4 v224, s[36:39], 0 offen lds
	s_add_i32 m0, s1, 0x6000
	s_mov_b32 s3, 0x10e000
	buffer_load_dwordx4 v223, s[36:39], 0 offen lds
	s_waitcnt vmcnt(4)
	s_waitcnt vmcnt(0)
	s_movk_i32 s4, 0x80
	v_cvt_pk_bf16_f32 v4, v110, v122
	v_cvt_pk_bf16_f32 v5, v126, v114
	v_cvt_pk_bf16_f32 v6, v118, v130
	v_cvt_pk_bf16_f32 v7, v138, v142
	ds_write_b128 v229, v[4:7] offset:32768
	v_cvt_pk_bf16_f32 v4, v111, v123
	v_cvt_pk_bf16_f32 v5, v127, v115
	v_cvt_pk_bf16_f32 v6, v119, v131
	v_cvt_pk_bf16_f32 v7, v139, v143
	ds_write_b128 v229, v[4:7] offset:32832
	v_cvt_pk_bf16_f32 v4, v112, v124
	v_cvt_pk_bf16_f32 v5, v128, v116
	v_cvt_pk_bf16_f32 v6, v120, v132
	v_cvt_pk_bf16_f32 v7, v140, v144
	ds_write_b128 v229, v[4:7] offset:32896
	v_cvt_pk_bf16_f32 v4, v113, v125
	v_cvt_pk_bf16_f32 v5, v129, v117
	v_cvt_pk_bf16_f32 v6, v121, v133
	v_cvt_pk_bf16_f32 v7, v141, v145
	ds_write_b128 v3, v[4:7] offset:32768
	buffer_load_dwordx4 v[4:7], v222, s[24:27], s67 offen
	buffer_load_dwordx4 v[8:11], v222, s[24:27], s68 offen
	buffer_load_dwordx4 v[12:15], v222, s[24:27], s69 offen
	buffer_load_dwordx4 v[16:19], v222, s[24:27], s70 offen
	buffer_load_dwordx4 v[20:23], v222, s[24:27], s71 offen
	buffer_load_dwordx4 v[28:31], v222, s[24:27], s76 offen
	buffer_load_dwordx4 v[24:27], v222, s[24:27], s77 offen
	buffer_load_dwordx4 v[32:35], v222, s[24:27], s78 offen
	s_waitcnt lgkmcnt(0)
	s_barrier
	v_mov_b32_e32 v37, v36
	v_mov_b32_e32 v38, v36
	v_mov_b32_e32 v39, v36
	v_mov_b32_e32 v40, v36
	v_mov_b32_e32 v41, v36
	v_mov_b32_e32 v42, v36
	v_mov_b32_e32 v43, v36
	v_mov_b32_e32 v44, v36
	v_mov_b32_e32 v45, v36
	v_mov_b32_e32 v46, v36
	v_mov_b32_e32 v47, v36
	v_mov_b32_e32 v48, v36
	v_mov_b32_e32 v49, v36
	v_mov_b32_e32 v50, v36
	v_mov_b32_e32 v51, v36
	v_mov_b32_e32 v52, v36
	v_mov_b32_e32 v53, v36
	v_mov_b32_e32 v54, v36
	v_mov_b32_e32 v55, v36
	v_mov_b32_e32 v56, v36
	v_mov_b32_e32 v57, v36
	v_mov_b32_e32 v58, v36
	v_mov_b32_e32 v59, v36
	v_mov_b32_e32 v60, v36
	v_mov_b32_e32 v61, v36
	v_mov_b32_e32 v62, v36
	v_mov_b32_e32 v63, v36
	v_mov_b32_e32 v64, v36
	v_mov_b32_e32 v65, v36
	v_mov_b32_e32 v66, v36
	v_mov_b32_e32 v67, v36
	v_mov_b32_e32 v68, v36
	v_mov_b32_e32 v69, v36
	v_mov_b32_e32 v70, v36
	v_mov_b32_e32 v71, v36
	v_mov_b32_e32 v72, v36
	v_mov_b32_e32 v73, v36
	v_mov_b32_e32 v74, v36
	v_mov_b32_e32 v75, v36
	v_mov_b32_e32 v76, v36
	v_mov_b32_e32 v77, v36
	v_mov_b32_e32 v78, v36
	v_mov_b32_e32 v79, v36
	v_mov_b32_e32 v80, v36
	v_mov_b32_e32 v81, v36
	v_mov_b32_e32 v82, v36
	v_mov_b32_e32 v83, v36
	v_mov_b32_e32 v84, v36
	v_mov_b32_e32 v85, v36
	v_mov_b32_e32 v86, v36
	v_mov_b32_e32 v87, v36
	v_mov_b32_e32 v88, v36
	v_mov_b32_e32 v89, v36
	v_mov_b32_e32 v90, v36
	v_mov_b32_e32 v91, v36
	v_mov_b32_e32 v92, v36
	v_mov_b32_e32 v93, v36
	v_mov_b32_e32 v94, v36
	v_mov_b32_e32 v95, v36
	v_mov_b32_e32 v96, v36
	v_mov_b32_e32 v97, v36
	v_mov_b32_e32 v98, v36
	v_mov_b32_e32 v99, v36
	v_mov_b32_e32 v100, v36
	v_mov_b32_e32 v101, v36
	v_mov_b32_e32 v102, v36
	v_mov_b32_e32 v103, v36
	v_mov_b32_e32 v104, v36
	v_mov_b32_e32 v105, v36
	v_mov_b32_e32 v106, v36
	v_mov_b32_e32 v107, v36
	v_mov_b32_e32 v108, v36
	v_mov_b32_e32 v109, v36
	v_mov_b32_e32 v110, v36
	v_mov_b32_e32 v111, v36
	v_mov_b32_e32 v112, v36
	v_mov_b32_e32 v113, v36
	v_mov_b32_e32 v114, v36
	v_mov_b32_e32 v115, v36
	v_mov_b32_e32 v116, v36
	v_mov_b32_e32 v117, v36
	v_mov_b32_e32 v118, v36
	v_mov_b32_e32 v119, v36
	v_mov_b32_e32 v120, v36
	v_mov_b32_e32 v121, v36
	v_mov_b32_e32 v122, v36
	v_mov_b32_e32 v123, v36
	v_mov_b32_e32 v124, v36
	v_mov_b32_e32 v125, v36
	v_mov_b32_e32 v126, v36
	v_mov_b32_e32 v127, v36
	v_mov_b32_e32 v128, v36
	v_mov_b32_e32 v129, v36
	v_mov_b32_e32 v130, v36
	v_mov_b32_e32 v131, v36
	v_mov_b32_e32 v132, v36
	v_mov_b32_e32 v133, v36
	v_mov_b32_e32 v134, v36
	v_mov_b32_e32 v135, v36
	v_mov_b32_e32 v136, v36
	v_mov_b32_e32 v137, v36
	v_mov_b32_e32 v138, v36
	v_mov_b32_e32 v139, v36
	v_mov_b32_e32 v140, v36
	v_mov_b32_e32 v141, v36
	v_mov_b32_e32 v142, v36
	v_mov_b32_e32 v143, v36
	v_mov_b32_e32 v144, v36
	v_mov_b32_e32 v145, v36
	v_mov_b32_e32 v146, v36
	v_mov_b32_e32 v147, v36
	v_mov_b32_e32 v148, v36
	v_mov_b32_e32 v149, v36
	v_mov_b32_e32 v150, v36
	v_mov_b32_e32 v151, v36
	v_mov_b32_e32 v152, v36
	v_mov_b32_e32 v153, v36
	v_mov_b32_e32 v154, v36
	v_mov_b32_e32 v155, v36
	v_mov_b32_e32 v156, v36
	v_mov_b32_e32 v157, v36
	v_mov_b32_e32 v158, v36
	v_mov_b32_e32 v159, v36
	v_mov_b32_e32 v160, v36
	v_mov_b32_e32 v161, v36
	v_mov_b32_e32 v162, v36
	v_mov_b32_e32 v163, v36
	.p2alignl 6, 3212836864
